# G5: ROWRS row-scale loads hoisted from epilogue to unit header (spare VGPRs), header panel_e and rowsrc round trips merged into one wait
# baseline (speedup 1.0000x reference)
;     __device__ bool next(int i, Unit& u) const {
;         const int nwg = npan * NT; const long L = (long)i * G + c; if (L >= nwg) return false;
;     __device__ __forceinline__ void operator()(const f32x4 (&acc)[2][2][4][2], const Unit& u, int wr, int wc, int fr, int fq) const {
;     ...
;                 for (int m = 0; m < 4; ++m) rs8[ai][m] = SS[row0 + ai * HALF + m * 16];
; template <class Epi, class Sched, bool ALIGN_EPI = false, bool SP2 = false>
; __device__ __forceinline__ void gemm_phase(PG8_LAS unsigned char* lds, const Gemm g, const Sched& S, const Epi& E, const bool skip_epi = false) {
;     ...
;         const bool has_next = S.next(ui + 1, nxt);
.LBB0_1719:
	s_lshl_b32 s4, s38, 8
	s_add_i32 s4, s4, s54
	v_or_b32_e32 v248, s4, v145
	v_ashrrev_i32_e32 v249, 31, v248
	v_lshl_add_u64 v[248:249], v[248:249], 2, s[18:19]
	global_load_dword v240, v[248:249], off offset:704
	global_load_dword v241, v[248:249], off offset:640
	global_load_dword v242, v[248:249], off offset:576
	global_load_dword v243, v[248:249], off offset:512
	global_load_dword v244, v[248:249], off offset:192
	global_load_dword v245, v[248:249], off offset:128
	global_load_dword v246, v[248:249], off offset:64
	global_load_dword v247, v[248:249], off
	s_add_i32 s53, s53, 1
	s_mul_i32 s4, s53, s57
	s_mul_hi_u32 s5, s53, s97
	s_add_i32 s5, s5, s4
	s_mul_i32 s4, s53, s97
	s_add_u32 s4, s4, s94
	s_addc_u32 s5, s5, s47
	v_cmp_ge_i64_e32 vcc, s[4:5], v[138:139]
	v_cmp_lt_i64_e64 s[6:7], s[4:5], v[138:139]
	s_cbranch_vccnz .LBB0_1725
	s_ashr_i32 s5, s4, 31
	s_lshr_b32 s5, s5, 29
	s_add_i32 s28, s4, s5
	s_and_b32 s5, s28, -8
	s_sub_i32 s29, s4, s5
	s_cmp_ge_i32 s29, s46
	s_mov_b64 s[4:5], -1
	s_cbranch_scc0 .LBB0_1722
	s_sub_i32 s4, s29, s46
	s_mul_i32 s4, s4, s3
	s_add_i32 s30, s4, s49
	s_mov_b64 s[4:5], 0

; #define PG8_GIDX(G_, PM_) do { if constexpr (Sched::GATHER) { _Pragma("unroll") for (int h_ = 0; h_ < 2; ++h_) _Pragma("unroll") for (int i_ = 0; i_ < 2; ++i_) { int R_, C_; stage_rc(tid * 16 + i_ * 8192, R_, C_); \
;         const int src_ = S.rowsrc[(PM_) * BM + h_ * HALF + R_]; G_[h_][i_] = (unsigned)(src_ * K + C_) * 2u; } } } while (0)
;     __device__ bool next(int i, Unit& u) const {
;     ...
;         const int nig = GP * NT, grp = wgid / nig, fm = grp * GP, gsz = (npan - fm) < GP ? (npan - fm) : GP; const int rr = wgid % nig;
;         const int p = fm + rr % gsz; u.pm = p; u.pn = panel_e[p] * NT + rr / gsz; u.ko = 0; return true;
; template <class Epi, class Sched, bool ALIGN_EPI = false, bool SP2 = false>
; __device__ __forceinline__ void gemm_phase(PG8_LAS unsigned char* lds, const Gemm g, const Sched& S, const Epi& E, const bool skip_epi = false) {
;     ...
;         if (has_next) PG8_GIDX(gN, nxt.pm);
.LBB0_1724:
	s_ashr_i32 s4, s28, 3
	s_add_i32 s4, s30, s4
	s_mul_hi_i32 s5, s4, 0x92492493
	s_add_i32 s5, s5, s4
	s_lshr_b32 s28, s5, 31
	s_ashr_i32 s5, s5, 6
	s_add_i32 s5, s5, s28
	s_lshl_b32 s28, s5, 2
	s_sub_i32 s29, s2, s28
	s_min_i32 s29, s29, 4
	s_abs_i32 s30, s29
	v_cvt_f32_u32_e32 v2, s30
	s_sub_i32 s34, 0, s30
	s_mulk_i32 s5, 0x70
	s_sub_i32 s4, s4, s5
	v_rcp_iflag_f32_e32 v2, v2
	s_abs_i32 s5, s4
	s_xor_b32 s31, s4, s29
	s_ashr_i32 s31, s31, 31
	v_mul_f32_e32 v2, 0x4f7ffffe, v2
	v_cvt_u32_f32_e32 v2, v2
	s_nop 0
	v_readfirstlane_b32 s35, v2
	s_mul_i32 s34, s34, s35
	s_mul_hi_u32 s34, s35, s34
	s_add_i32 s35, s35, s34
	s_mul_hi_u32 s34, s5, s35
	s_mul_i32 s35, s34, s30
	s_sub_i32 s5, s5, s35
	s_add_i32 s42, s34, 1
	s_sub_i32 s35, s5, s30
	s_cmp_ge_u32 s5, s30
	s_cselect_b32 s34, s42, s34
	s_cselect_b32 s5, s35, s5
	s_add_i32 s35, s34, 1
	s_cmp_ge_u32 s5, s30
	s_cselect_b32 s5, s35, s34
	s_xor_b32 s5, s5, s31
	s_sub_i32 s30, s5, s31
	s_mul_i32 s5, s30, s29
	s_sub_i32 s4, s4, s5
	s_add_i32 s28, s28, s4
	s_ashr_i32 s29, s28, 31
	s_lshl_b64 s[4:5], s[28:29], 2
	s_add_u32 s4, s14, s4
	s_addc_u32 s5, s15, s5
	global_load_dword v250, v133, s[4:5]
.LBB0_1725:
	s_nop 0
	v_cndmask_b32_e64 v2, 0, 1, s[6:7]
	v_cmp_ne_u32_e64 s[4:5], 1, v2
	s_andn2_b64 vcc, exec, s[6:7]
	s_cbranch_vccnz .LBB0_1727
	s_lshl_b32 s29, s28, 8
	v_add_u32_e32 v2, s29, v1
	v_add_u32_e32 v4, s29, v151
	s_bitset1_b32 s29, 7
	v_ashrrev_i32_e32 v3, 31, v2
	v_ashrrev_i32_e32 v5, 31, v4
	v_add_u32_e32 v6, s29, v1
	v_add_u32_e32 v8, s29, v151
	v_lshl_add_u64 v[2:3], v[2:3], 2, s[20:21]
	v_lshl_add_u64 v[4:5], v[4:5], 2, s[20:21]
	v_ashrrev_i32_e32 v7, 31, v6
	v_ashrrev_i32_e32 v9, 31, v8
	v_lshl_add_u64 v[6:7], v[6:7], 2, s[20:21]
	v_lshl_add_u64 v[8:9], v[8:9], 2, s[20:21]
	global_load_dword v2, v[2:3], off
	s_nop 0
	global_load_dword v3, v[4:5], off
	s_nop 0
	global_load_dword v4, v[6:7], off
	global_load_dword v5, v[8:9], off
	s_waitcnt vmcnt(0)
	v_readfirstlane_b32 s29, v250
	v_lshl_add_u32 v164, v2, 11, v152
	v_lshl_add_u32 v163, v3, 11, v153
	v_lshl_add_u32 v162, v4, 11, v152
	v_lshl_add_u32 v161, v5, 11, v153
	s_mul_i32 s29, s29, 28
	s_add_i32 s30, s29, s30

; __device__ __forceinline__ unsigned cvt_pk_bf16(float lo, float hi) { const f32x2c_t v = {lo, hi}; return __builtin_bit_cast(unsigned, __builtin_convertvector(v, bf16x2c_t)); }
; __device__ __forceinline__ float silu_f(float a) { return a * __builtin_amdgcn_rcpf(1.0f + __builtin_amdgcn_exp2f(a * -1.4426950408889634f)); }
;     __device__ __forceinline__ void operator()(const f32x4 (&acc)[2][2][4][2], const Unit& u, int wr, int wc, int fr, int fq) const {
;         const int row0 = u.pm * BM + wr * 64 + fr; const int pnl = MOE ? (u.pn % 28) : u.pn;
;         const int lane = fr + 16 * fq, qs4 = QSRC_ST(lane); const int rowS = u.pm * BM + wr * 64 + (lane >> 2), colS = pnl * HALF + wc * 32 + 8 * (lane & 3);
;         float rs8[2][4];
;         if constexpr (MOE) {
; #pragma unroll
;             for (int ai = 0; ai < 2; ++ai)
; #pragma unroll
;                 for (int m = 0; m < 4; ++m) rs8[ai][m] = SS[row0 + ai * HALF + m * 16];
;             asm volatile("" : "+v"(rs8[0][0]), "+v"(rs8[0][1]), "+v"(rs8[0][2]), "+v"(rs8[0][3]), "+v"(rs8[1][0]), "+v"(rs8[1][1]), "+v"(rs8[1][2]), "+v"(rs8[1][3]));
;         } else rstd8(SS, u.pm * BM + wr * 64, lane, rs8);
; #pragma unroll
;         for (int ai = 0; ai < 2; ++ai) {
; #pragma unroll
;             for (int m = 0; m < 4; ++m) { const int row = row0 + ai * HALF + m * 16; const float rs = rs8[ai][m];
;                 const f32x4 a0 = acc[ai][0][m][0] * rs, a1 = acc[ai][0][m][1] * rs, b0 = acc[ai][1][m][0] * rs, b1 = acc[ai][1][m][1] * rs;
;                 f32x4 g0, g1;
; #pragma unroll
;                 for (int j = 0; j < 4; ++j) { g0[j] = silu_f(a0[j]) * b0[j]; g1[j] = silu_f(a1[j]) * b1[j]; }
;                 u32x4 w; w.x = cvt_pk_bf16(g0[0], g0[1]); w.y = cvt_pk_bf16(g0[2], g0[3]); w.z = cvt_pk_bf16(g1[0], g1[1]); w.w = cvt_pk_bf16(g1[2], g1[3]);
;                 w = lane_perm(w, qs4); u32x4* dst = (u32x4*)(O + (size_t)(rowS + ai * HALF + m * 16) * ldo + colS); (void)row;
;                 if constexpr (MOE) __builtin_nontemporal_store(w, dst); else *dst = w; } }
.LBB0_1731:
	s_lshl_b32 s6, s38, 8
	s_add_i32 s6, s6, s54
	v_mov_b32_e32 v130, v240
	v_mov_b32_e32 v132, v241
	v_mov_b32_e32 v144, v242
	v_mov_b32_e32 v146, v243
	v_mov_b32_e32 v148, v244
	v_mov_b32_e32 v150, v245
	v_mov_b32_e32 v166, v246
	v_mov_b32_e32 v168, v247
	s_mul_hi_i32 s7, s36, 0x92492493
	v_readlane_b32 s40, v254, 36
	s_add_i32 s7, s7, s36
	v_readlane_b32 s41, v254, 37
	v_or_b32_e32 v147, s6, v155
	s_lshr_b32 s6, s7, 31
	s_lshr_b32 s7, s7, 4
	v_mov_b64_e32 v[140:141], s[40:41]
	s_add_i32 s29, s7, s6
	v_mad_i64_i32 v[170:171], s[6:7], v147, s60, v[140:141]
	s_mul_i32 s29, s29, 28
	s_sub_i32 s6, s36, s29
	v_lshl_or_b32 v142, s6, 7, v157
	v_ashrrev_i32_e32 v143, 31, v142
	v_lshlrev_b64 v[142:143], 1, v[142:143]
	v_lshl_add_u64 v[170:171], v[170:171], 0, v[142:143]
	s_and_b64 vcc, exec, s[4:5]
	s_mov_b64 s[4:5], -1
	s_waitcnt vmcnt(0)
	s_nop 0
	v_pk_mul_f32 v[126:127], v[126:127], v[168:169] op_sel_hi:[1,0]
	v_pk_mul_f32 v[128:129], v[128:129], v[168:169] op_sel_hi:[1,0]
	v_pk_mul_f32 v[118:119], v[118:119], v[168:169] op_sel_hi:[1,0]
	v_pk_mul_f32 v[122:123], v[122:123], v[168:169] op_sel_hi:[1,0]
	v_pk_mul_f32 v[114:115], v[114:115], v[168:169] op_sel_hi:[1,0]
	v_pk_mul_f32 v[120:121], v[120:121], v[168:169] op_sel_hi:[1,0]
	v_pk_mul_f32 v[124:125], v[124:125], v[168:169] op_sel_hi:[1,0]
	v_pk_mul_f32 v[116:117], v[116:117], v[168:169] op_sel_hi:[1,0]
	v_pk_mul_f32 v[110:111], v[110:111], v[166:167] op_sel_hi:[1,0]
	v_mul_f32_e32 v149, 0xbfb8aa3b, v126
	v_mul_f32_e32 v165, 0xbfb8aa3b, v127
	v_mul_f32_e32 v169, 0xbfb8aa3b, v128
	v_mul_f32_e32 v172, 0xbfb8aa3b, v129
	v_pk_mul_f32 v[102:103], v[102:103], v[166:167] op_sel_hi:[1,0]
	v_pk_mul_f32 v[106:107], v[106:107], v[166:167] op_sel_hi:[1,0]
	v_mul_f32_e32 v167, 0xbfb8aa3b, v122
	v_mul_f32_e32 v168, 0xbfb8aa3b, v123
	v_mul_f32_e32 v174, 0xbfb8aa3b, v125
	v_mul_f32_e32 v175, 0xbfb8aa3b, v110
	v_exp_f32_e32 v149, v149
	v_exp_f32_e32 v165, v165
	v_exp_f32_e32 v169, v169
	v_exp_f32_e32 v172, v172
	v_mul_f32_e32 v173, 0xbfb8aa3b, v124
	v_mul_f32_e32 v176, 0xbfb8aa3b, v111
	v_exp_f32_e32 v167, v167
	v_exp_f32_e32 v168, v168
	v_exp_f32_e32 v174, v174
	v_exp_f32_e32 v175, v175
	v_exp_f32_e32 v173, v173
	v_exp_f32_e32 v176, v176
	v_mul_f32_e32 v178, 0xbfb8aa3b, v107
	v_add_f32_e32 v149, 1.0, v149
	v_add_f32_e32 v165, 1.0, v165
	v_add_f32_e32 v179, 1.0, v169
	v_add_f32_e32 v181, 1.0, v172
	v_exp_f32_e32 v180, v178
	v_add_f32_e32 v167, 1.0, v167
	v_add_f32_e32 v178, 1.0, v168
	v_add_f32_e32 v183, 1.0, v174
	v_add_f32_e32 v184, 1.0, v175
	v_rcp_f32_e32 v168, v149
	v_rcp_f32_e32 v169, v165
	v_rcp_f32_e32 v174, v179
	v_rcp_f32_e32 v175, v181
	v_add_f32_e32 v182, 1.0, v173
	v_add_f32_e32 v185, 1.0, v176
	v_rcp_f32_e32 v172, v167
	v_rcp_f32_e32 v173, v178
	v_mul_f32_e32 v177, 0xbfb8aa3b, v106
	v_rcp_f32_e32 v178, v184
	v_rcp_f32_e32 v179, v185
	v_exp_f32_e32 v177, v177
	v_pk_mul_f32 v[126:127], v[126:127], v[168:169]
	v_pk_mul_f32 v[128:129], v[128:129], v[174:175]
	v_pk_mul_f32 v[122:123], v[122:123], v[172:173]
	v_pk_mul_f32 v[118:119], v[118:119], v[126:127]
	v_pk_mul_f32 v[120:121], v[120:121], v[128:129]
	v_pk_mul_f32 v[114:115], v[114:115], v[122:123]
	v_cvt_pk_bf16_f32 v118, v118, v119
	v_cvt_pk_bf16_f32 v119, v120, v121
	v_pk_mul_f32 v[110:111], v[110:111], v[178:179]
	v_add_f32_e32 v186, 1.0, v177
	v_cvt_pk_bf16_f32 v120, v114, v115
	ds_bpermute_b32 v115, v156, v119
	v_add_f32_e32 v119, 1.0, v180
	v_pk_mul_f32 v[102:103], v[102:103], v[110:111]
	v_pk_mul_f32 v[110:111], v[112:113], v[166:167] op_sel_hi:[1,0]
	ds_bpermute_b32 v114, v156, v118
	v_rcp_f32_e32 v118, v186
	v_rcp_f32_e32 v119, v119
	v_mul_f32_e32 v112, 0xbfb8aa3b, v110
	v_mul_f32_e32 v113, 0xbfb8aa3b, v111
	v_exp_f32_e32 v112, v112
	v_exp_f32_e32 v113, v113
	v_pk_mul_f32 v[106:107], v[106:107], v[118:119]
	v_pk_mul_f32 v[98:99], v[98:99], v[166:167] op_sel_hi:[1,0]
	v_pk_mul_f32 v[108:109], v[108:109], v[166:167] op_sel_hi:[1,0]
	v_pk_mul_f32 v[98:99], v[98:99], v[106:107]
	v_add_f32_e32 v106, 1.0, v112
	v_add_f32_e32 v107, 1.0, v113
	v_mul_f32_e32 v112, 0xbfb8aa3b, v108
	v_mul_f32_e32 v113, 0xbfb8aa3b, v109
	v_exp_f32_e32 v112, v112
	v_exp_f32_e32 v113, v113
	v_rcp_f32_e32 v106, v106
	v_rcp_f32_e32 v107, v107
	v_add_f32_e32 v112, 1.0, v112
	v_add_f32_e32 v113, 1.0, v113
	v_rcp_f32_e32 v112, v112
	v_rcp_f32_e32 v113, v113
	v_pk_mul_f32 v[106:107], v[110:111], v[106:107]
	v_pk_mul_f32 v[104:105], v[104:105], v[166:167] op_sel_hi:[1,0]
	v_pk_mul_f32 v[100:101], v[100:101], v[166:167] op_sel_hi:[1,0]
	v_pk_mul_f32 v[104:105], v[104:105], v[106:107]
	v_pk_mul_f32 v[106:107], v[108:109], v[112:113]
	v_cvt_pk_bf16_f32 v102, v102, v103
	v_pk_mul_f32 v[100:101], v[100:101], v[106:107]
	v_cvt_pk_bf16_f32 v103, v104, v105
	v_cvt_pk_bf16_f32 v104, v98, v99
	v_cvt_pk_bf16_f32 v101, v100, v101
	v_pk_mul_f32 v[94:95], v[94:95], v[150:151] op_sel_hi:[1,0]
	ds_bpermute_b32 v98, v156, v102
	ds_bpermute_b32 v99, v156, v103
	ds_bpermute_b32 v100, v156, v104
	ds_bpermute_b32 v101, v156, v101
	v_mul_f32_e32 v104, 0xbfb8aa3b, v94
	v_mul_f32_e32 v105, 0xbfb8aa3b, v95
	v_exp_f32_e32 v104, v104
	v_exp_f32_e32 v105, v105
	v_or_b32_e32 v102, 16, v147
	v_mad_i64_i32 v[102:103], s[6:7], v102, s60, v[140:141]
	v_lshl_add_u64 v[102:103], v[102:103], 0, v[142:143]
	s_waitcnt lgkmcnt(0)
; __device__ __forceinline__ unsigned cvt_pk_bf16(float lo, float hi) { const f32x2c_t v = {lo, hi}; return __builtin_bit_cast(unsigned, __builtin_convertvector(v, bf16x2c_t)); }
; __device__ __forceinline__ float silu_f(float a) { return a * __builtin_amdgcn_rcpf(1.0f + __builtin_amdgcn_exp2f(a * -1.4426950408889634f)); }
;     __device__ __forceinline__ void operator()(const f32x4 (&acc)[2][2][4][2], const Unit& u, int wr, int wc, int fr, int fq) const {
;     ...
;             for (int m = 0; m < 4; ++m) { const int row = row0 + ai * HALF + m * 16; const float rs = rs8[ai][m];
;                 const f32x4 a0 = acc[ai][0][m][0] * rs, a1 = acc[ai][0][m][1] * rs, b0 = acc[ai][1][m][0] * rs, b1 = acc[ai][1][m][1] * rs;
;                 f32x4 g0, g1;
; #pragma unroll
;                 for (int j = 0; j < 4; ++j) { g0[j] = silu_f(a0[j]) * b0[j]; g1[j] = silu_f(a1[j]) * b1[j]; }
;                 u32x4 w; w.x = cvt_pk_bf16(g0[0], g0[1]); w.y = cvt_pk_bf16(g0[2], g0[3]); w.z = cvt_pk_bf16(g1[0], g1[1]); w.w = cvt_pk_bf16(g1[2], g1[3]);
;                 w = lane_perm(w, qs4); u32x4* dst = (u32x4*)(O + (size_t)(rowS + ai * HALF + m * 16) * ldo + colS); (void)row;
;                 if constexpr (MOE) __builtin_nontemporal_store(w, dst); else *dst = w; } }
	global_store_dwordx4 v[102:103], v[98:101], off nt
	v_pk_mul_f32 v[90:91], v[90:91], v[150:151] op_sel_hi:[1,0]
	v_pk_mul_f32 v[86:87], v[86:87], v[150:151] op_sel_hi:[1,0]
	v_add_f32_e32 v98, 1.0, v104
	v_add_f32_e32 v99, 1.0, v105
	v_rcp_f32_e32 v98, v98
	v_mul_f32_e32 v100, 0xbfb8aa3b, v90
	v_mul_f32_e32 v101, 0xbfb8aa3b, v91
	v_rcp_f32_e32 v99, v99
	v_exp_f32_e32 v100, v100
	v_exp_f32_e32 v101, v101
	v_pk_mul_f32 v[82:83], v[82:83], v[150:151] op_sel_hi:[1,0]
	v_pk_mul_f32 v[94:95], v[94:95], v[98:99]
	v_add_f32_e32 v100, 1.0, v100
	v_add_f32_e32 v101, 1.0, v101
	v_pk_mul_f32 v[86:87], v[86:87], v[94:95]
	v_pk_mul_f32 v[94:95], v[96:97], v[150:151] op_sel_hi:[1,0]
	v_rcp_f32_e32 v100, v100
	v_rcp_f32_e32 v101, v101
	v_mul_f32_e32 v96, 0xbfb8aa3b, v94
	v_mul_f32_e32 v97, 0xbfb8aa3b, v95
	v_exp_f32_e32 v96, v96
	v_exp_f32_e32 v97, v97
	v_pk_mul_f32 v[90:91], v[90:91], v[100:101]
	v_pk_mul_f32 v[92:93], v[92:93], v[150:151] op_sel_hi:[1,0]
	v_pk_mul_f32 v[82:83], v[82:83], v[90:91]
	v_add_f32_e32 v90, 1.0, v96
	v_add_f32_e32 v91, 1.0, v97
	v_mul_f32_e32 v96, 0xbfb8aa3b, v92
	v_mul_f32_e32 v97, 0xbfb8aa3b, v93
	v_exp_f32_e32 v96, v96
	v_exp_f32_e32 v97, v97
	v_rcp_f32_e32 v90, v90
	v_rcp_f32_e32 v91, v91
	v_add_f32_e32 v96, 1.0, v96
	v_add_f32_e32 v97, 1.0, v97
	v_rcp_f32_e32 v96, v96
	v_rcp_f32_e32 v97, v97
	v_pk_mul_f32 v[90:91], v[94:95], v[90:91]
	v_pk_mul_f32 v[88:89], v[88:89], v[150:151] op_sel_hi:[1,0]
	v_pk_mul_f32 v[84:85], v[84:85], v[150:151] op_sel_hi:[1,0]
	v_pk_mul_f32 v[88:89], v[88:89], v[90:91]
	v_pk_mul_f32 v[90:91], v[92:93], v[96:97]
	v_cvt_pk_bf16_f32 v86, v86, v87
	v_pk_mul_f32 v[84:85], v[84:85], v[90:91]
	v_cvt_pk_bf16_f32 v87, v88, v89
	v_cvt_pk_bf16_f32 v88, v82, v83
	v_cvt_pk_bf16_f32 v85, v84, v85
	v_pk_mul_f32 v[78:79], v[78:79], v[148:149] op_sel_hi:[1,0]
	ds_bpermute_b32 v82, v156, v86
	ds_bpermute_b32 v83, v156, v87
	ds_bpermute_b32 v84, v156, v88
	ds_bpermute_b32 v85, v156, v85
	v_mul_f32_e32 v88, 0xbfb8aa3b, v78
	v_mul_f32_e32 v89, 0xbfb8aa3b, v79
	v_exp_f32_e32 v88, v88
	v_exp_f32_e32 v89, v89
	v_or_b32_e32 v86, 32, v147
	v_mad_i64_i32 v[86:87], s[6:7], v86, s60, v[140:141]
	v_lshl_add_u64 v[86:87], v[86:87], 0, v[142:143]
	s_waitcnt lgkmcnt(0)
	global_store_dwordx4 v[86:87], v[82:85], off nt
	v_pk_mul_f32 v[74:75], v[74:75], v[148:149] op_sel_hi:[1,0]
	v_pk_mul_f32 v[70:71], v[70:71], v[148:149] op_sel_hi:[1,0]
	v_add_f32_e32 v82, 1.0, v88
	v_add_f32_e32 v83, 1.0, v89
	v_rcp_f32_e32 v82, v82
	v_mul_f32_e32 v84, 0xbfb8aa3b, v74
	v_mul_f32_e32 v85, 0xbfb8aa3b, v75
	v_rcp_f32_e32 v83, v83
	v_exp_f32_e32 v84, v84
	v_exp_f32_e32 v85, v85
	v_pk_mul_f32 v[66:67], v[66:67], v[148:149] op_sel_hi:[1,0]
	v_pk_mul_f32 v[78:79], v[78:79], v[82:83]
	v_add_f32_e32 v84, 1.0, v84
	v_add_f32_e32 v85, 1.0, v85
	v_pk_mul_f32 v[70:71], v[70:71], v[78:79]
	v_pk_mul_f32 v[78:79], v[80:81], v[148:149] op_sel_hi:[1,0]
	v_rcp_f32_e32 v84, v84
	v_rcp_f32_e32 v85, v85
	v_mul_f32_e32 v80, 0xbfb8aa3b, v78
	v_mul_f32_e32 v81, 0xbfb8aa3b, v79
	v_exp_f32_e32 v80, v80
	v_exp_f32_e32 v81, v81
	v_pk_mul_f32 v[74:75], v[74:75], v[84:85]
	v_pk_mul_f32 v[76:77], v[76:77], v[148:149] op_sel_hi:[1,0]
	v_pk_mul_f32 v[66:67], v[66:67], v[74:75]
	v_add_f32_e32 v74, 1.0, v80
	v_add_f32_e32 v75, 1.0, v81
	v_mul_f32_e32 v80, 0xbfb8aa3b, v76
	v_mul_f32_e32 v81, 0xbfb8aa3b, v77
	v_exp_f32_e32 v80, v80
	v_exp_f32_e32 v81, v81
	v_rcp_f32_e32 v74, v74
	v_rcp_f32_e32 v75, v75
	v_add_f32_e32 v80, 1.0, v80
	v_add_f32_e32 v81, 1.0, v81
	v_rcp_f32_e32 v80, v80
	v_rcp_f32_e32 v81, v81
	v_pk_mul_f32 v[74:75], v[78:79], v[74:75]
	v_pk_mul_f32 v[72:73], v[72:73], v[148:149] op_sel_hi:[1,0]
	v_pk_mul_f32 v[68:69], v[68:69], v[148:149] op_sel_hi:[1,0]
	v_pk_mul_f32 v[72:73], v[72:73], v[74:75]
	v_pk_mul_f32 v[74:75], v[76:77], v[80:81]
	v_cvt_pk_bf16_f32 v70, v70, v71
	v_pk_mul_f32 v[68:69], v[68:69], v[74:75]
	v_cvt_pk_bf16_f32 v71, v72, v73
	v_cvt_pk_bf16_f32 v72, v66, v67
	v_cvt_pk_bf16_f32 v69, v68, v69
	ds_bpermute_b32 v66, v156, v70
	ds_bpermute_b32 v67, v156, v71
	ds_bpermute_b32 v68, v156, v72
	ds_bpermute_b32 v69, v156, v69
	v_or_b32_e32 v70, 48, v147
	v_mad_i64_i32 v[70:71], s[6:7], v70, s60, v[140:141]
	v_lshl_add_u64 v[70:71], v[70:71], 0, v[142:143]
	v_pk_mul_f32 v[62:63], v[62:63], v[146:147] op_sel_hi:[1,0]
	s_waitcnt lgkmcnt(0)
	global_store_dwordx4 v[70:71], v[66:69], off nt
	v_pk_mul_f32 v[58:59], v[58:59], v[146:147] op_sel_hi:[1,0]
	v_pk_mul_f32 v[50:51], v[50:51], v[146:147] op_sel_hi:[1,0]
	v_mul_f32_e32 v66, 0xbfb8aa3b, v62
	v_mul_f32_e32 v67, 0xbfb8aa3b, v63
	v_exp_f32_e32 v66, v66
	v_exp_f32_e32 v67, v67
	v_mul_f32_e32 v68, 0xbfb8aa3b, v58
	v_mul_f32_e32 v69, 0xbfb8aa3b, v59
	v_add_f32_e32 v66, 1.0, v66
	v_add_f32_e32 v67, 1.0, v67
	v_rcp_f32_e32 v66, v66
	v_rcp_f32_e32 v67, v67
	v_exp_f32_e32 v68, v68
	v_exp_f32_e32 v69, v69
	v_pk_mul_f32 v[42:43], v[42:43], v[146:147] op_sel_hi:[1,0]
	v_pk_mul_f32 v[62:63], v[62:63], v[66:67]
	v_add_f32_e32 v68, 1.0, v68
	v_add_f32_e32 v69, 1.0, v69
	v_pk_mul_f32 v[50:51], v[50:51], v[62:63]
	v_pk_mul_f32 v[62:63], v[64:65], v[146:147] op_sel_hi:[1,0]
	v_rcp_f32_e32 v68, v68
	v_rcp_f32_e32 v69, v69
	v_mul_f32_e32 v64, 0xbfb8aa3b, v62
	v_mul_f32_e32 v65, 0xbfb8aa3b, v63
	v_exp_f32_e32 v64, v64
	v_exp_f32_e32 v65, v65
	v_pk_mul_f32 v[58:59], v[58:59], v[68:69]
	v_pk_mul_f32 v[60:61], v[60:61], v[146:147] op_sel_hi:[1,0]
	v_pk_mul_f32 v[42:43], v[42:43], v[58:59]
	v_add_f32_e32 v58, 1.0, v64
	v_add_f32_e32 v59, 1.0, v65
	v_mul_f32_e32 v64, 0xbfb8aa3b, v60
	v_mul_f32_e32 v65, 0xbfb8aa3b, v61
	v_exp_f32_e32 v64, v64
	v_exp_f32_e32 v65, v65
	v_rcp_f32_e32 v58, v58
	v_rcp_f32_e32 v59, v59
	v_add_f32_e32 v64, 1.0, v64
	v_add_f32_e32 v65, 1.0, v65
	v_rcp_f32_e32 v64, v64
	v_rcp_f32_e32 v65, v65
	v_pk_mul_f32 v[58:59], v[62:63], v[58:59]
	v_pk_mul_f32 v[52:53], v[52:53], v[146:147] op_sel_hi:[1,0]
	v_pk_mul_f32 v[44:45], v[44:45], v[146:147] op_sel_hi:[1,0]
	v_pk_mul_f32 v[52:53], v[52:53], v[58:59]
	v_pk_mul_f32 v[58:59], v[60:61], v[64:65]
	v_cvt_pk_bf16_f32 v50, v50, v51
	v_pk_mul_f32 v[44:45], v[44:45], v[58:59]
	v_cvt_pk_bf16_f32 v51, v52, v53
	v_cvt_pk_bf16_f32 v52, v42, v43
	v_cvt_pk_bf16_f32 v45, v44, v45
	ds_bpermute_b32 v42, v156, v50
	ds_bpermute_b32 v43, v156, v51
	ds_bpermute_b32 v44, v156, v52
	ds_bpermute_b32 v45, v156, v45
	v_add_u32_e32 v70, 0x80, v147
	v_mad_i64_i32 v[50:51], s[6:7], v70, s60, v[140:141]
	v_lshl_add_u64 v[50:51], v[50:51], 0, v[142:143]
	v_pk_mul_f32 v[34:35], v[34:35], v[144:145] op_sel_hi:[1,0]
	s_waitcnt lgkmcnt(0)
; __device__ __forceinline__ unsigned cvt_pk_bf16(float lo, float hi) { const f32x2c_t v = {lo, hi}; return __builtin_bit_cast(unsigned, __builtin_convertvector(v, bf16x2c_t)); }
; __device__ __forceinline__ float silu_f(float a) { return a * __builtin_amdgcn_rcpf(1.0f + __builtin_amdgcn_exp2f(a * -1.4426950408889634f)); }
; #define PG8_BAR __builtin_amdgcn_s_barrier()
;     __device__ __forceinline__ void operator()(const f32x4 (&acc)[2][2][4][2], const Unit& u, int wr, int wc, int fr, int fq) const {
;     ...
;             for (int m = 0; m < 4; ++m) { const int row = row0 + ai * HALF + m * 16; const float rs = rs8[ai][m];
;                 const f32x4 a0 = acc[ai][0][m][0] * rs, a1 = acc[ai][0][m][1] * rs, b0 = acc[ai][1][m][0] * rs, b1 = acc[ai][1][m][1] * rs;
;                 f32x4 g0, g1;
; #pragma unroll
;                 for (int j = 0; j < 4; ++j) { g0[j] = silu_f(a0[j]) * b0[j]; g1[j] = silu_f(a1[j]) * b1[j]; }
;                 u32x4 w; w.x = cvt_pk_bf16(g0[0], g0[1]); w.y = cvt_pk_bf16(g0[2], g0[3]); w.z = cvt_pk_bf16(g1[0], g1[1]); w.w = cvt_pk_bf16(g1[2], g1[3]);
;                 w = lane_perm(w, qs4); u32x4* dst = (u32x4*)(O + (size_t)(rowS + ai * HALF + m * 16) * ldo + colS); (void)row;
;                 if constexpr (MOE) __builtin_nontemporal_store(w, dst); else *dst = w; } }
; template <class Epi, class Sched, bool ALIGN_EPI = false, bool SP2 = false>
; __device__ __forceinline__ void gemm_phase(PG8_LAS unsigned char* lds, const Gemm g, const Sched& S, const Epi& E, const bool skip_epi = false) {
;     ...
;         if (!has_next) break;
; #pragma unroll
;         for (int a = 0; a < 2; ++a)
; #pragma unroll
;             for (int b = 0; b < 2; ++b)
; #pragma unroll
;                 for (int m = 0; m < 4; ++m)
; #pragma unroll
;                     for (int n = 0; n < 2; ++n) acc[a][b][m][n] = (f32x4){0.f, 0.f, 0.f, 0.f};
;         cur = nxt; cA = nA; cB = nB; ++ui;
;         if constexpr (Sched::GATHER) { gA[0][0] = gN[0][0]; gA[0][1] = gN[0][1]; gA[1][0] = gN[1][0]; gA[1][1] = gN[1][1]; }
;         if constexpr (ALIGN_EPI) { if (wr == 1) PG8_BAR; }
;     }
	global_store_dwordx4 v[50:51], v[42:45], off nt
	v_pk_mul_f32 v[38:39], v[38:39], v[144:145] op_sel_hi:[1,0]
	v_pk_mul_f32 v[40:41], v[40:41], v[144:145] op_sel_hi:[1,0]
	v_mul_f32_e32 v44, 0xbfb8aa3b, v34
	v_mul_f32_e32 v45, 0xbfb8aa3b, v35
	v_exp_f32_e32 v44, v44
	v_exp_f32_e32 v45, v45
	v_mul_f32_e32 v52, 0xbfb8aa3b, v38
	v_mul_f32_e32 v53, 0xbfb8aa3b, v39
	v_exp_f32_e32 v52, v52
	v_exp_f32_e32 v53, v53
	v_add_f32_e32 v44, 1.0, v44
	v_add_f32_e32 v45, 1.0, v45
	v_rcp_f32_e32 v44, v44
	v_rcp_f32_e32 v45, v45
	v_add_f32_e32 v42, 1.0, v52
	v_add_f32_e32 v43, 1.0, v53
	v_rcp_f32_e32 v42, v42
	v_rcp_f32_e32 v43, v43
	v_pk_mul_f32 v[34:35], v[34:35], v[44:45]
	v_mul_f32_e32 v44, 0xbfb8aa3b, v40
	v_mul_f32_e32 v45, 0xbfb8aa3b, v41
	v_exp_f32_e32 v44, v44
	v_exp_f32_e32 v45, v45
	v_pk_mul_f32 v[38:39], v[38:39], v[42:43]
	v_pk_mul_f32 v[42:43], v[54:55], v[144:145] op_sel_hi:[1,0]
	v_pk_mul_f32 v[36:37], v[36:37], v[144:145] op_sel_hi:[1,0]
	v_pk_mul_f32 v[38:39], v[42:43], v[38:39]
	v_pk_mul_f32 v[42:43], v[46:47], v[144:145] op_sel_hi:[1,0]
	v_cvt_pk_bf16_f32 v38, v38, v39
	v_pk_mul_f32 v[34:35], v[42:43], v[34:35]
	v_add_f32_e32 v42, 1.0, v44
	v_add_f32_e32 v43, 1.0, v45
	v_mul_f32_e32 v44, 0xbfb8aa3b, v36
	v_mul_f32_e32 v45, 0xbfb8aa3b, v37
	v_exp_f32_e32 v44, v44
	v_exp_f32_e32 v45, v45
	v_rcp_f32_e32 v42, v42
	v_rcp_f32_e32 v43, v43
	v_add_f32_e32 v44, 1.0, v44
	v_add_f32_e32 v45, 1.0, v45
	v_rcp_f32_e32 v44, v44
	v_rcp_f32_e32 v45, v45
	v_pk_mul_f32 v[40:41], v[40:41], v[42:43]
	v_pk_mul_f32 v[42:43], v[56:57], v[144:145] op_sel_hi:[1,0]
	v_pk_mul_f32 v[22:23], v[22:23], v[132:133] op_sel_hi:[1,0]
	v_pk_mul_f32 v[40:41], v[42:43], v[40:41]
	v_pk_mul_f32 v[36:37], v[36:37], v[44:45]
	v_pk_mul_f32 v[42:43], v[48:49], v[144:145] op_sel_hi:[1,0]
	v_cvt_pk_bf16_f32 v39, v40, v41
	v_pk_mul_f32 v[36:37], v[42:43], v[36:37]
	v_cvt_pk_bf16_f32 v40, v34, v35
	v_cvt_pk_bf16_f32 v37, v36, v37
	ds_bpermute_b32 v34, v156, v38
	ds_bpermute_b32 v35, v156, v39
	ds_bpermute_b32 v36, v156, v40
	ds_bpermute_b32 v37, v156, v37
	v_mul_f32_e32 v40, 0xbfb8aa3b, v22
	v_mul_f32_e32 v41, 0xbfb8aa3b, v23
	v_exp_f32_e32 v40, v40
	v_exp_f32_e32 v41, v41
	v_add_u32_e32 v38, 0x90, v147
	v_mad_i64_i32 v[38:39], s[6:7], v38, s60, v[140:141]
	v_lshl_add_u64 v[38:39], v[38:39], 0, v[142:143]
	v_pk_mul_f32 v[18:19], v[18:19], v[132:133] op_sel_hi:[1,0]
	s_waitcnt lgkmcnt(0)
	global_store_dwordx4 v[38:39], v[34:37], off nt
	v_pk_mul_f32 v[30:31], v[30:31], v[132:133] op_sel_hi:[1,0]
	v_pk_mul_f32 v[24:25], v[24:25], v[132:133] op_sel_hi:[1,0]
	v_add_f32_e32 v34, 1.0, v40
	v_add_f32_e32 v35, 1.0, v41
	v_mul_f32_e32 v36, 0xbfb8aa3b, v18
	v_mul_f32_e32 v37, 0xbfb8aa3b, v19
	v_rcp_f32_e32 v34, v34
	v_exp_f32_e32 v36, v36
	v_exp_f32_e32 v37, v37
	v_rcp_f32_e32 v35, v35
	v_pk_mul_f32 v[26:27], v[26:27], v[132:133] op_sel_hi:[1,0]
	v_add_f32_e32 v36, 1.0, v36
	v_add_f32_e32 v37, 1.0, v37
	v_pk_mul_f32 v[22:23], v[22:23], v[34:35]
	v_rcp_f32_e32 v36, v36
	v_rcp_f32_e32 v37, v37
	v_pk_mul_f32 v[22:23], v[30:31], v[22:23]
	v_mul_f32_e32 v30, 0xbfb8aa3b, v24
	v_mul_f32_e32 v31, 0xbfb8aa3b, v25
	v_exp_f32_e32 v30, v30
	v_exp_f32_e32 v31, v31
	v_pk_mul_f32 v[18:19], v[18:19], v[36:37]
	v_pk_mul_f32 v[20:21], v[20:21], v[132:133] op_sel_hi:[1,0]
	v_pk_mul_f32 v[18:19], v[26:27], v[18:19]
	v_add_f32_e32 v26, 1.0, v30
	v_add_f32_e32 v27, 1.0, v31
	v_mul_f32_e32 v30, 0xbfb8aa3b, v20
	v_mul_f32_e32 v31, 0xbfb8aa3b, v21
	v_exp_f32_e32 v30, v30
	v_exp_f32_e32 v31, v31
	v_rcp_f32_e32 v26, v26
	v_rcp_f32_e32 v27, v27
	v_add_f32_e32 v30, 1.0, v30
	v_add_f32_e32 v31, 1.0, v31
	v_rcp_f32_e32 v30, v30
	v_rcp_f32_e32 v31, v31
	v_pk_mul_f32 v[24:25], v[24:25], v[26:27]
	v_pk_mul_f32 v[26:27], v[32:33], v[132:133] op_sel_hi:[1,0]
	v_cvt_pk_bf16_f32 v22, v22, v23
	v_pk_mul_f32 v[24:25], v[26:27], v[24:25]
	v_pk_mul_f32 v[20:21], v[20:21], v[30:31]
	v_pk_mul_f32 v[26:27], v[28:29], v[132:133] op_sel_hi:[1,0]
	v_cvt_pk_bf16_f32 v23, v24, v25
	v_pk_mul_f32 v[20:21], v[26:27], v[20:21]
	v_cvt_pk_bf16_f32 v24, v18, v19
	v_cvt_pk_bf16_f32 v21, v20, v21
	v_pk_mul_f32 v[6:7], v[6:7], v[130:131] op_sel_hi:[1,0]
	ds_bpermute_b32 v18, v156, v22
	ds_bpermute_b32 v19, v156, v23
	ds_bpermute_b32 v20, v156, v24
	ds_bpermute_b32 v21, v156, v21
	v_mul_f32_e32 v24, 0xbfb8aa3b, v6
	v_mul_f32_e32 v25, 0xbfb8aa3b, v7
	v_exp_f32_e32 v24, v24
	v_exp_f32_e32 v25, v25
	v_add_u32_e32 v22, 0xa0, v147
	v_mad_i64_i32 v[22:23], s[6:7], v22, s60, v[140:141]
	v_lshl_add_u64 v[22:23], v[22:23], 0, v[142:143]
	v_pk_mul_f32 v[2:3], v[2:3], v[130:131] op_sel_hi:[1,0]
	s_waitcnt lgkmcnt(0)
	global_store_dwordx4 v[22:23], v[18:21], off nt
	v_pk_mul_f32 v[14:15], v[14:15], v[130:131] op_sel_hi:[1,0]
	v_pk_mul_f32 v[8:9], v[8:9], v[130:131] op_sel_hi:[1,0]
	v_add_f32_e32 v18, 1.0, v24
	v_add_f32_e32 v19, 1.0, v25
	v_mul_f32_e32 v20, 0xbfb8aa3b, v2
	v_mul_f32_e32 v21, 0xbfb8aa3b, v3
	v_rcp_f32_e32 v18, v18
	v_exp_f32_e32 v20, v20
	v_exp_f32_e32 v21, v21
	v_rcp_f32_e32 v19, v19
	v_pk_mul_f32 v[10:11], v[10:11], v[130:131] op_sel_hi:[1,0]
	v_add_f32_e32 v20, 1.0, v20
	v_add_f32_e32 v21, 1.0, v21
	v_pk_mul_f32 v[6:7], v[6:7], v[18:19]
	v_rcp_f32_e32 v20, v20
	v_rcp_f32_e32 v21, v21
	v_pk_mul_f32 v[6:7], v[14:15], v[6:7]
	v_mul_f32_e32 v14, 0xbfb8aa3b, v8
	v_mul_f32_e32 v15, 0xbfb8aa3b, v9
	v_exp_f32_e32 v14, v14
	v_exp_f32_e32 v15, v15
	v_pk_mul_f32 v[2:3], v[2:3], v[20:21]
	v_pk_mul_f32 v[4:5], v[4:5], v[130:131] op_sel_hi:[1,0]
	v_pk_mul_f32 v[2:3], v[10:11], v[2:3]
	v_add_f32_e32 v10, 1.0, v14
	v_add_f32_e32 v11, 1.0, v15
	v_mul_f32_e32 v14, 0xbfb8aa3b, v4
	v_mul_f32_e32 v15, 0xbfb8aa3b, v5
	v_exp_f32_e32 v14, v14
	v_exp_f32_e32 v15, v15
	v_rcp_f32_e32 v10, v10
	v_rcp_f32_e32 v11, v11
	v_add_f32_e32 v14, 1.0, v14
	v_add_f32_e32 v15, 1.0, v15
	v_rcp_f32_e32 v176, v182
	v_rcp_f32_e32 v177, v183
	v_rcp_f32_e32 v14, v14
	v_rcp_f32_e32 v15, v15
	v_pk_mul_f32 v[8:9], v[8:9], v[10:11]
	v_pk_mul_f32 v[10:11], v[16:17], v[130:131] op_sel_hi:[1,0]
	v_pk_mul_f32 v[124:125], v[124:125], v[176:177]
	v_pk_mul_f32 v[8:9], v[10:11], v[8:9]
	v_pk_mul_f32 v[4:5], v[4:5], v[14:15]
	v_pk_mul_f32 v[10:11], v[12:13], v[130:131] op_sel_hi:[1,0]
	v_pk_mul_f32 v[116:117], v[116:117], v[124:125]
	v_pk_mul_f32 v[4:5], v[10:11], v[4:5]
	v_cvt_pk_bf16_f32 v117, v116, v117
	v_cvt_pk_bf16_f32 v6, v6, v7
	v_cvt_pk_bf16_f32 v7, v8, v9
	v_cvt_pk_bf16_f32 v8, v2, v3
	v_cvt_pk_bf16_f32 v5, v4, v5
	ds_bpermute_b32 v116, v156, v120
	ds_bpermute_b32 v117, v156, v117
	ds_bpermute_b32 v2, v156, v6
	ds_bpermute_b32 v3, v156, v7
	ds_bpermute_b32 v4, v156, v8
	ds_bpermute_b32 v5, v156, v5
	v_add_u32_e32 v6, 0xb0, v147
	v_mad_i64_i32 v[6:7], s[6:7], v6, s60, v[140:141]
	v_lshl_add_u64 v[6:7], v[6:7], 0, v[142:143]
	s_waitcnt lgkmcnt(4)
	global_store_dwordx4 v[170:171], v[114:117], off nt
	s_waitcnt lgkmcnt(0)
	global_store_dwordx4 v[6:7], v[2:5], off nt
	s_cbranch_vccnz .LBB0_1718
	s_andn2_b64 vcc, exec, s[10:11]
	s_cbranch_vccnz .LBB0_1717
	s_barrier
	s_branch .LBB0_1717
